# P23 last K-iteration: only two epilogue rows carried, in the load part of segment 4; its MFMA block left free of VALU
# baseline (speedup 1.0000x reference)
.Lh23_last:
	v_mov_b32_e32 v172, v177
	ds_read_b128 v[164:167], v196 offset:49152
	ds_read_b128 v[168:171], v196 offset:50176
	ds_read_b128 v[198:201], v196 offset:51200
	ds_read_b128 v[202:205], v196 offset:52224
	ds_read_b128 v[214:217], v196 offset:53248
	ds_read_b128 v[218:221], v196 offset:54272
	ds_read_b128 v[222:225], v196 offset:55296
	ds_read_b128 v[226:229], v196 offset:56320
	s_mov_b32 m0, s58
	v_add_u32_e32 v172, s85, v172
	global_load_lds_dwordx4 v172, s[6:7]
	v_mov_b32_e32 v172, v177
	s_add_i32 s85, s85, s48
	v_add_u32_e32 v172, s85, v172
	s_mov_b32 m0, s59
	s_add_i32 s85, s85, s48
	global_load_lds_dwordx4 v172, s[6:7]
	v_mov_b32_e32 v172, v177
	s_mov_b32 m0, s62
	v_add_u32_e32 v172, s85, v172
	global_load_lds_dwordx4 v172, s[6:7]
	v_mov_b32_e32 v172, v177
	s_add_i32 s85, s85, s48
	v_add_u32_e32 v172, s85, v172
	s_mov_b32 m0, s63
	s_nop 0
	global_load_lds_dwordx4 v172, s[6:7]
	v_mov_b32_e32 v172, v176
	s_mov_b32 m0, s60
	v_add_u32_e32 v172, s84, v172
	global_load_lds_dwordx4 v172, s[4:5]
	v_mov_b32_e32 v172, v176
	s_add_i32 s84, s84, s47
	v_add_u32_e32 v172, s84, v172
	s_mov_b32 m0, s61
	s_nop 0
	global_load_lds_dwordx4 v172, s[4:5]
	s_mul_hi_i32 s25, s81, 0x2e8ba2e9
	s_lshr_b32 s28, s25, 31
	s_lshr_b32 s25, s25, 3
	s_add_i32 s25, s25, s28
	s_mul_i32 s25, s25, 44
	s_sub_i32 s25, s81, s25
	s_lshl_b32 s28, s25, 7
	s_lshl_b32 s24, s24, 8
	s_add_i32 s24, s24, s66
	s_mul_i32 s24, s24, s71
	s_add_i32 s24, s24, s28
	s_add_i32 s24, s24, s8
	s_add_u32 s100, s12, s24
	s_addc_u32 s101, s13, 0
	s_mov_b32 s98, 0xbfb8aa3b
	v_mul_u32_u24_e32 v206, s71, v178
	v_lshl_add_u32 v206, v179, 3, v206
	v_pk_fma_f32 v[158:159], v[158:159], s[18:19], 0 op_sel_hi:[1,0,0]
	v_pk_fma_f32 v[160:161], v[160:161], s[18:19], 0 op_sel_hi:[1,0,0]
	v_pk_fma_f32 v[154:155], v[154:155], s[18:19], 0 op_sel_hi:[1,0,0]
	v_pk_fma_f32 v[156:157], v[156:157], s[18:19], 0 op_sel_hi:[1,0,0]
	v_pk_fma_f32 v[142:143], v[142:143], s[20:21], 0 op_sel_hi:[1,0,0]
	v_pk_fma_f32 v[144:145], v[144:145], s[20:21], 0 op_sel_hi:[1,0,0]
	v_pk_fma_f32 v[134:135], v[134:135], s[20:21], 0 op_sel_hi:[1,0,0]
	v_pk_fma_f32 v[136:137], v[136:137], s[20:21], 0 op_sel_hi:[1,0,0]
	v_pk_fma_f32 v[150:151], v[150:151], s[18:19], 0 op_sel_hi:[1,0,0]
	v_pk_fma_f32 v[152:153], v[152:153], s[18:19], 0 op_sel_hi:[1,0,0]
	v_pk_fma_f32 v[146:147], v[146:147], s[18:19], 0 op_sel_hi:[1,0,0]
	v_pk_fma_f32 v[148:149], v[148:149], s[18:19], 0 op_sel_hi:[1,0,0]
	v_pk_fma_f32 v[126:127], v[126:127], s[20:21], 0 op_sel_hi:[1,0,0]
	v_pk_fma_f32 v[128:129], v[128:129], s[20:21], 0 op_sel_hi:[1,0,0]
	v_pk_fma_f32 v[118:119], v[118:119], s[20:21], 0 op_sel_hi:[1,0,0]
	v_pk_fma_f32 v[120:121], v[120:121], s[20:21], 0 op_sel_hi:[1,0,0]
	v_pk_mul_f32 v[230:231], v[158:159], s[98:99] op_sel_hi:[1,0]
	v_pk_mul_f32 v[232:233], v[160:161], s[98:99] op_sel_hi:[1,0]
	v_pk_mul_f32 v[234:235], v[154:155], s[98:99] op_sel_hi:[1,0]
	v_pk_mul_f32 v[236:237], v[156:157], s[98:99] op_sel_hi:[1,0]
	v_pk_mul_f32 v[238:239], v[150:151], s[98:99] op_sel_hi:[1,0]
	v_pk_mul_f32 v[240:241], v[152:153], s[98:99] op_sel_hi:[1,0]
	v_pk_mul_f32 v[242:243], v[146:147], s[98:99] op_sel_hi:[1,0]
	v_pk_mul_f32 v[244:245], v[148:149], s[98:99] op_sel_hi:[1,0]
	v_exp_f32_e32 v230, v230
	v_exp_f32_e32 v231, v231
	v_exp_f32_e32 v232, v232
	v_exp_f32_e32 v233, v233
	v_exp_f32_e32 v234, v234
	v_exp_f32_e32 v235, v235
	v_exp_f32_e32 v236, v236
	v_exp_f32_e32 v237, v237
	v_exp_f32_e32 v238, v238
	v_exp_f32_e32 v239, v239
	v_exp_f32_e32 v240, v240
	v_exp_f32_e32 v241, v241
	v_exp_f32_e32 v242, v242
	v_exp_f32_e32 v243, v243
	v_exp_f32_e32 v244, v244
	v_exp_f32_e32 v245, v245
	v_pk_add_f32 v[230:231], v[230:231], 1.0 op_sel_hi:[1,0]
	v_pk_add_f32 v[232:233], v[232:233], 1.0 op_sel_hi:[1,0]
	v_pk_add_f32 v[234:235], v[234:235], 1.0 op_sel_hi:[1,0]
	v_pk_add_f32 v[236:237], v[236:237], 1.0 op_sel_hi:[1,0]
	v_pk_add_f32 v[238:239], v[238:239], 1.0 op_sel_hi:[1,0]
	v_pk_add_f32 v[240:241], v[240:241], 1.0 op_sel_hi:[1,0]
	v_pk_add_f32 v[242:243], v[242:243], 1.0 op_sel_hi:[1,0]
	v_pk_add_f32 v[244:245], v[244:245], 1.0 op_sel_hi:[1,0]
	v_rcp_f32_e32 v230, v230
	v_rcp_f32_e32 v231, v231
	v_rcp_f32_e32 v232, v232
	v_rcp_f32_e32 v233, v233
	v_rcp_f32_e32 v234, v234
	v_rcp_f32_e32 v235, v235
	v_rcp_f32_e32 v236, v236
	v_rcp_f32_e32 v237, v237
	v_rcp_f32_e32 v238, v238
	v_rcp_f32_e32 v239, v239
	v_rcp_f32_e32 v240, v240
	v_rcp_f32_e32 v241, v241
	v_rcp_f32_e32 v242, v242
	v_rcp_f32_e32 v243, v243
	v_rcp_f32_e32 v244, v244
	v_rcp_f32_e32 v245, v245
	v_pk_mul_f32 v[230:231], v[158:159], v[230:231]
	v_pk_mul_f32 v[232:233], v[160:161], v[232:233]
	v_pk_mul_f32 v[234:235], v[154:155], v[234:235]
	v_pk_mul_f32 v[236:237], v[156:157], v[236:237]
	v_pk_mul_f32 v[238:239], v[150:151], v[238:239]
	v_pk_mul_f32 v[240:241], v[152:153], v[240:241]
	v_pk_mul_f32 v[242:243], v[146:147], v[242:243]
	v_pk_mul_f32 v[244:245], v[148:149], v[244:245]
	v_pk_mul_f32 v[142:143], v[142:143], v[230:231]
	v_pk_mul_f32 v[144:145], v[144:145], v[232:233]
	v_pk_mul_f32 v[134:135], v[134:135], v[234:235]
	v_pk_mul_f32 v[136:137], v[136:137], v[236:237]
	v_pk_mul_f32 v[126:127], v[126:127], v[238:239]
	v_pk_mul_f32 v[128:129], v[128:129], v[240:241]
	v_pk_mul_f32 v[118:119], v[118:119], v[242:243]
	v_pk_mul_f32 v[120:121], v[120:121], v[244:245]
	v_med3_f32 v142, v142, s72, v197
	v_med3_f32 v143, v143, s72, v197
	v_med3_f32 v144, v144, s72, v197
	v_med3_f32 v145, v145, s72, v197
	v_med3_f32 v134, v134, s72, v197
	v_med3_f32 v135, v135, s72, v197
	v_med3_f32 v136, v136, s72, v197
	v_med3_f32 v137, v137, s72, v197
	v_med3_f32 v126, v126, s72, v197
	v_med3_f32 v127, v127, s72, v197
	v_med3_f32 v128, v128, s72, v197
	v_med3_f32 v129, v129, s72, v197
	v_med3_f32 v118, v118, s72, v197
	v_med3_f32 v119, v119, s72, v197
	v_med3_f32 v120, v120, s72, v197
	v_med3_f32 v121, v121, s72, v197
	v_cvt_pk_fp8_f32 v246, v142, v143
	v_cvt_pk_fp8_f32 v247, v134, v135
	v_cvt_pk_fp8_f32 v248, v126, v127
	v_cvt_pk_fp8_f32 v249, v118, v119
	v_add_u32_e32 v208, s57, v206
	v_cvt_pk_fp8_f32 v246, v144, v145 op_sel:[0,0,1]
	v_cvt_pk_fp8_f32 v247, v136, v137 op_sel:[0,0,1]
	v_cvt_pk_fp8_f32 v248, v128, v129 op_sel:[0,0,1]
	v_cvt_pk_fp8_f32 v249, v120, v121 op_sel:[0,0,1]
	s_nop 1
	global_store_dwordx2 v206, v[246:247], s[100:101]
	global_store_dwordx2 v208, v[248:249], s[100:101]
	s_waitcnt vmcnt(10)
	s_waitcnt lgkmcnt(0)
	s_barrier
	s_setprio 1
	s_waitcnt lgkmcnt(0)
	v_mfma_f32_16x16x128_f8f6f4 v[94:97], v[2:9], v[164:171], v[94:97]
	v_mfma_f32_16x16x128_f8f6f4 v[90:93], v[10:17], v[164:171], v[90:93]
	v_mfma_f32_16x16x128_f8f6f4 v[86:89], v[2:9], v[198:205], v[86:89]
	v_mfma_f32_16x16x128_f8f6f4 v[82:85], v[10:17], v[198:205], v[82:85]
	v_mfma_f32_16x16x128_f8f6f4 v[74:77], v[2:9], v[214:221], v[74:77]
	v_mfma_f32_16x16x128_f8f6f4 v[66:69], v[10:17], v[214:221], v[66:69]
	v_mfma_f32_16x16x128_f8f6f4 v[58:61], v[2:9], v[222:229], v[58:61]
	v_mfma_f32_16x16x128_f8f6f4 v[50:53], v[10:17], v[222:229], v[50:53]
	s_setprio 0
	s_setprio 1
	v_mfma_f32_16x16x128_f8f6f4 v[78:81], v[18:25], v[164:171], v[78:81]
	v_mfma_f32_16x16x128_f8f6f4 v[70:73], v[26:33], v[164:171], v[70:73]
	v_mfma_f32_16x16x128_f8f6f4 v[62:65], v[18:25], v[198:205], v[62:65]
	v_mfma_f32_16x16x128_f8f6f4 v[54:57], v[26:33], v[198:205], v[54:57]
	v_mfma_f32_16x16x128_f8f6f4 v[46:49], v[18:25], v[214:221], v[46:49]
	v_mfma_f32_16x16x128_f8f6f4 v[42:45], v[26:33], v[214:221], v[42:45]
	v_mfma_f32_16x16x128_f8f6f4 v[38:41], v[18:25], v[222:229], v[38:41]
	v_mfma_f32_16x16x128_f8f6f4 v[34:37], v[26:33], v[222:229], v[34:37]
	s_setprio 0
	s_barrier
	s_and_b64 vcc, exec, s[16:17]
	s_cbranch_vccz .Lh23_nb
	s_barrier

.Lh23_epi0:
	v_pk_fma_f32 v[138:139], v[138:139], s[18:19], 0 op_sel_hi:[1,0,0]
	v_pk_fma_f32 v[140:141], v[140:141], s[18:19], 0 op_sel_hi:[1,0,0]
	v_pk_fma_f32 v[130:131], v[130:131], s[18:19], 0 op_sel_hi:[1,0,0]
	v_pk_fma_f32 v[132:133], v[132:133], s[18:19], 0 op_sel_hi:[1,0,0]
	v_pk_fma_f32 v[110:111], v[110:111], s[20:21], 0 op_sel_hi:[1,0,0]
	v_pk_fma_f32 v[112:113], v[112:113], s[20:21], 0 op_sel_hi:[1,0,0]
	v_pk_fma_f32 v[106:107], v[106:107], s[20:21], 0 op_sel_hi:[1,0,0]
	v_pk_fma_f32 v[108:109], v[108:109], s[20:21], 0 op_sel_hi:[1,0,0]
	v_pk_fma_f32 v[122:123], v[122:123], s[18:19], 0 op_sel_hi:[1,0,0]
	v_pk_fma_f32 v[124:125], v[124:125], s[18:19], 0 op_sel_hi:[1,0,0]
	v_pk_fma_f32 v[114:115], v[114:115], s[18:19], 0 op_sel_hi:[1,0,0]
	v_pk_fma_f32 v[116:117], v[116:117], s[18:19], 0 op_sel_hi:[1,0,0]
	v_pk_fma_f32 v[102:103], v[102:103], s[20:21], 0 op_sel_hi:[1,0,0]
	v_pk_fma_f32 v[104:105], v[104:105], s[20:21], 0 op_sel_hi:[1,0,0]
	v_pk_fma_f32 v[98:99], v[98:99], s[20:21], 0 op_sel_hi:[1,0,0]
	v_pk_fma_f32 v[100:101], v[100:101], s[20:21], 0 op_sel_hi:[1,0,0]
	v_pk_mul_f32 v[230:231], v[138:139], s[98:99] op_sel_hi:[1,0]
	v_pk_mul_f32 v[232:233], v[140:141], s[98:99] op_sel_hi:[1,0]
	v_pk_mul_f32 v[234:235], v[130:131], s[98:99] op_sel_hi:[1,0]
	v_pk_mul_f32 v[236:237], v[132:133], s[98:99] op_sel_hi:[1,0]
	v_pk_mul_f32 v[238:239], v[122:123], s[98:99] op_sel_hi:[1,0]
	v_pk_mul_f32 v[240:241], v[124:125], s[98:99] op_sel_hi:[1,0]
	v_pk_mul_f32 v[242:243], v[114:115], s[98:99] op_sel_hi:[1,0]
	v_pk_mul_f32 v[244:245], v[116:117], s[98:99] op_sel_hi:[1,0]
	v_exp_f32_e32 v230, v230
	v_exp_f32_e32 v231, v231
	v_exp_f32_e32 v232, v232
	v_exp_f32_e32 v233, v233
	v_exp_f32_e32 v234, v234
	v_exp_f32_e32 v235, v235
	v_exp_f32_e32 v236, v236
	v_exp_f32_e32 v237, v237
	v_exp_f32_e32 v238, v238
	v_exp_f32_e32 v239, v239
	v_exp_f32_e32 v240, v240
	v_exp_f32_e32 v241, v241
	v_exp_f32_e32 v242, v242
	v_exp_f32_e32 v243, v243
	v_exp_f32_e32 v244, v244
	v_exp_f32_e32 v245, v245
	v_pk_add_f32 v[230:231], v[230:231], 1.0 op_sel_hi:[1,0]
	v_pk_add_f32 v[232:233], v[232:233], 1.0 op_sel_hi:[1,0]
	v_pk_add_f32 v[234:235], v[234:235], 1.0 op_sel_hi:[1,0]
	v_pk_add_f32 v[236:237], v[236:237], 1.0 op_sel_hi:[1,0]
	v_pk_add_f32 v[238:239], v[238:239], 1.0 op_sel_hi:[1,0]
	v_pk_add_f32 v[240:241], v[240:241], 1.0 op_sel_hi:[1,0]
	v_pk_add_f32 v[242:243], v[242:243], 1.0 op_sel_hi:[1,0]
	v_pk_add_f32 v[244:245], v[244:245], 1.0 op_sel_hi:[1,0]
	v_rcp_f32_e32 v230, v230
	v_rcp_f32_e32 v231, v231
	v_rcp_f32_e32 v232, v232
	v_rcp_f32_e32 v233, v233
	v_rcp_f32_e32 v234, v234
	v_rcp_f32_e32 v235, v235
	v_rcp_f32_e32 v236, v236
	v_rcp_f32_e32 v237, v237
	v_rcp_f32_e32 v238, v238
	v_rcp_f32_e32 v239, v239
	v_rcp_f32_e32 v240, v240
	v_rcp_f32_e32 v241, v241
	v_rcp_f32_e32 v242, v242
	v_rcp_f32_e32 v243, v243
	v_rcp_f32_e32 v244, v244
	v_rcp_f32_e32 v245, v245
	v_pk_mul_f32 v[230:231], v[138:139], v[230:231]
	v_pk_mul_f32 v[232:233], v[140:141], v[232:233]
	v_pk_mul_f32 v[234:235], v[130:131], v[234:235]
	v_pk_mul_f32 v[236:237], v[132:133], v[236:237]
	v_pk_mul_f32 v[238:239], v[122:123], v[238:239]
	v_pk_mul_f32 v[240:241], v[124:125], v[240:241]
	v_pk_mul_f32 v[242:243], v[114:115], v[242:243]
	v_pk_mul_f32 v[244:245], v[116:117], v[244:245]
	v_pk_mul_f32 v[110:111], v[110:111], v[230:231]
	v_pk_mul_f32 v[112:113], v[112:113], v[232:233]
	v_pk_mul_f32 v[106:107], v[106:107], v[234:235]
	v_pk_mul_f32 v[108:109], v[108:109], v[236:237]
	v_pk_mul_f32 v[102:103], v[102:103], v[238:239]
	v_pk_mul_f32 v[104:105], v[104:105], v[240:241]
	v_pk_mul_f32 v[98:99], v[98:99], v[242:243]
	v_pk_mul_f32 v[100:101], v[100:101], v[244:245]
	v_med3_f32 v110, v110, s72, v197
	v_med3_f32 v111, v111, s72, v197
	v_med3_f32 v112, v112, s72, v197
	v_med3_f32 v113, v113, s72, v197
	v_med3_f32 v106, v106, s72, v197
	v_med3_f32 v107, v107, s72, v197
	v_med3_f32 v108, v108, s72, v197
	v_med3_f32 v109, v109, s72, v197
	v_med3_f32 v102, v102, s72, v197
	v_med3_f32 v103, v103, s72, v197
	v_med3_f32 v104, v104, s72, v197
	v_med3_f32 v105, v105, s72, v197
	v_med3_f32 v98, v98, s72, v197
	v_med3_f32 v99, v99, s72, v197
	v_med3_f32 v100, v100, s72, v197
	v_med3_f32 v101, v101, s72, v197
	v_cvt_pk_fp8_f32 v250, v110, v111
	v_cvt_pk_fp8_f32 v251, v106, v107
	v_cvt_pk_fp8_f32 v252, v102, v103
	v_cvt_pk_fp8_f32 v253, v98, v99
	v_add_u32_e32 v207, s73, v206
	v_add_u32_e32 v208, s74, v206
	v_cvt_pk_fp8_f32 v250, v112, v113 op_sel:[0,0,1]
	v_cvt_pk_fp8_f32 v251, v108, v109 op_sel:[0,0,1]
	v_cvt_pk_fp8_f32 v252, v104, v105 op_sel:[0,0,1]
	v_cvt_pk_fp8_f32 v253, v100, v101 op_sel:[0,0,1]
	s_nop 1
	global_store_dwordx2 v207, v[250:251], s[100:101]
	global_store_dwordx2 v208, v[252:253], s[100:101]
